# attention: next unit's first Q/K/V cache lines touched (5 dword loads into dead registers) during the previous unit's final key step, so the unit start-up loads hit L2; placement as v052
# baseline (speedup 1.0000x reference)
.LBB0_339:
	v_add_u32_e32 v2, s33, v242
	ds_read_b64_tr_b16 v[194:195], v2 offset:24576
	ds_read_b64_tr_b16 v[196:197], v2 offset:25088
	s_waitcnt lgkmcnt(9)
	v_mfma_f32_32x32x16_bf16 v[82:97], v[170:173], v[154:157], v[100:115]
	ds_read_b64_tr_b16 v[170:171], v2 offset:28672
	ds_read_b64_tr_b16 v[172:173], v2 offset:29184
	s_waitcnt lgkmcnt(10)
	v_mfma_f32_32x32x16_bf16 v[100:115], v[162:165], v[154:157], v[100:115]
	ds_read_b64_tr_b16 v[124:125], v2 offset:25600
	ds_read_b64_tr_b16 v[126:127], v2 offset:26112
	s_waitcnt lgkmcnt(11)
	v_mfma_f32_32x32x16_bf16 v[82:97], v[174:177], v[150:153], v[82:97]
	ds_read_b64_tr_b16 v[120:121], v2 offset:29696
	ds_read_b64_tr_b16 v[122:123], v2 offset:30208
	s_waitcnt lgkmcnt(12)
	v_mfma_f32_32x32x16_bf16 v[100:115], v[166:169], v[150:153], v[100:115]
	ds_read_b64_tr_b16 v[116:117], v2 offset:26624
	ds_read_b64_tr_b16 v[118:119], v2 offset:27136
	s_waitcnt lgkmcnt(13)
	v_mfma_f32_32x32x16_bf16 v[82:97], v[182:185], v[146:149], v[82:97]
	ds_read_b64_tr_b16 v[12:13], v2 offset:30720
	ds_read_b64_tr_b16 v[14:15], v2 offset:31232
	s_waitcnt lgkmcnt(14)
	v_mfma_f32_32x32x16_bf16 v[100:115], v[178:181], v[146:149], v[100:115]
	ds_read_b64_tr_b16 v[8:9], v2 offset:27648
	ds_read_b64_tr_b16 v[10:11], v2 offset:28160
	s_waitcnt lgkmcnt(14)
	v_mfma_f32_32x32x16_bf16 v[82:97], v[190:193], v[142:145], v[82:97]
	ds_read_b64_tr_b16 v[4:5], v2 offset:31744
	ds_read_b64_tr_b16 v[6:7], v2 offset:32256
	v_mfma_f32_32x32x16_bf16 v[100:115], v[186:189], v[142:145], v[100:115]
	s_cmp_lt_u32 s21, 3
	s_cbranch_scc0 .Lpf_skip_l0
	v_readfirstlane_b32 s98, v0
	s_add_i32 s99, s21, 1
	s_lshr_b32 vcc_hi, s99, 1
	s_lshl_b32 vcc_hi, vcc_hi, 7
	s_bitcmp0_b32 s99, 0
	s_cselect_b32 s99, s49, s48
	s_ashr_i32 s98, s98, 6
	s_mul_i32 vcc_lo, s4, 0x4800000
	s_lshl_b32 s99, s99, 8
	s_lshl_b32 s100, s4, 14
	s_add_i32 s99, s99, s100
	s_lshl_b32 s100, s98, 5
	s_add_i32 s99, s99, s100
	s_mul_i32 s99, s99, 0x1200
	s_add_u32 s100, s52, vcc_hi
	s_addc_u32 s101, s53, 0
	s_add_u32 s100, s100, s99
	s_addc_u32 s101, s101, 0
	v_and_b32_e32 v244, 31, v0
	v_mul_u32_u24_e32 v244, 0x1200, v244
	v_bfe_u32 v245, v0, 5, 1
	v_lshl_or_b32 v244, v245, 4, v244
	global_load_dword v198, v244, s[100:101]
	s_add_u32 s100, s54, vcc_hi
	s_addc_u32 s101, s55, 0
	s_add_u32 s100, s100, vcc_lo
	s_addc_u32 s101, s101, 0
	s_lshl_b32 s99, s98, 4
	s_add_u32 s100, s100, s99
	s_addc_u32 s101, s101, 0
	v_and_b32_e32 v245, 63, v0
	v_mul_u32_u24_e32 v245, 0x1200, v245
	global_load_dword v199, v245, s[100:101]
	s_add_u32 s100, s100, 0x48000
	s_addc_u32 s101, s101, 0
	global_load_dword v200, v245, s[100:101]
	s_add_u32 s100, s62, vcc_lo
	s_addc_u32 s101, s63, 0
	s_lshr_b32 s99, s98, 2
	s_lshl_b32 s99, s99, 6
	s_add_u32 s100, s100, s99
	s_addc_u32 s101, s101, 0
	s_and_b32 s99, s98, 3
	s_lshl_b32 s99, s99, 4
	v_bfe_u32 v246, v0, 2, 4
	v_add_u32_e32 v246, s99, v246
	v_mul_u32_u24_e32 v246, 0x1200, v246
	v_and_b32_e32 v247, 3, v0
	v_lshl_add_u32 v246, v247, 4, v246
	global_load_dword v201, v246, s[100:101]
	global_load_dword v202, v246, s[100:101] offset:128
.Lpf_skip_l0:
	v_or_b32_e32 v17, 0xe0, v239
	v_or_b32_e32 v16, 0xc0, v239
	v_cmp_le_i32_e32 vcc, v17, v238
	s_nop 8
	v_cndmask_b32_e32 v99, v227, v100, vcc
	v_cmp_lt_i32_e32 vcc, v16, v238
	s_nop 1
	v_cndmask_b32_e32 v83, v227, v83, vcc
	v_cmp_le_i32_e32 vcc, v16, v238
	v_or_b32_e32 v16, 0xe1, v239
	s_nop 0
	v_cndmask_b32_e32 v82, v227, v82, vcc
	v_cmp_le_i32_e32 vcc, v16, v238
	v_or_b32_e32 v16, 0xc2, v239
	s_nop 0
	v_cndmask_b32_e32 v100, v227, v101, vcc
	v_cmp_le_i32_e32 vcc, v16, v238
	v_or_b32_e32 v16, 0xe2, v239
	s_nop 0
	v_cndmask_b32_e32 v101, v227, v84, vcc
	v_cmp_le_i32_e32 vcc, v16, v238
	v_or_b32_e32 v16, 0xc3, v239
	s_nop 0
	v_cndmask_b32_e32 v142, v227, v102, vcc
	v_cmp_le_i32_e32 vcc, v16, v238
	v_or_b32_e32 v16, 0xe3, v239
	s_nop 0
	v_cndmask_b32_e32 v143, v227, v85, vcc
	v_cmp_le_i32_e32 vcc, v16, v238
	v_or_b32_e32 v16, 0xc8, v239
	s_nop 0
	v_cndmask_b32_e32 v144, v227, v103, vcc
	v_cmp_le_i32_e32 vcc, v16, v238
	v_or_b32_e32 v16, 0xe8, v239
	s_nop 0
	v_cndmask_b32_e32 v102, v227, v86, vcc
	v_cmp_le_i32_e32 vcc, v16, v238
	v_or_b32_e32 v16, 0xc9, v239
	s_nop 0
	v_cndmask_b32_e32 v86, v227, v104, vcc
	v_cmp_le_i32_e32 vcc, v16, v238
	v_or_b32_e32 v16, 0xe9, v239
	s_nop 0
	v_cndmask_b32_e32 v103, v227, v87, vcc
	v_cmp_le_i32_e32 vcc, v16, v238
	v_or_b32_e32 v16, 0xca, v239
	s_nop 0
	v_cndmask_b32_e32 v87, v227, v105, vcc
	v_cmp_le_i32_e32 vcc, v16, v238
	v_or_b32_e32 v16, 0xea, v239
	s_nop 0
	v_cndmask_b32_e32 v104, v227, v88, vcc
	v_cmp_le_i32_e32 vcc, v16, v238
	v_or_b32_e32 v16, 0xcb, v239
	s_nop 0
	v_cndmask_b32_e32 v88, v227, v106, vcc
	v_cmp_le_i32_e32 vcc, v16, v238
	v_or_b32_e32 v16, 0xeb, v239
	s_nop 0
	v_cndmask_b32_e32 v105, v227, v89, vcc
	v_cmp_le_i32_e32 vcc, v16, v238
	v_or_b32_e32 v16, 0xd0, v239
	s_nop 0
	v_cndmask_b32_e32 v89, v227, v107, vcc
	v_cmp_le_i32_e32 vcc, v16, v238
	v_or_b32_e32 v16, 0xf0, v239
	s_nop 0
	v_cndmask_b32_e32 v106, v227, v90, vcc
	v_cmp_le_i32_e32 vcc, v16, v238
	v_or_b32_e32 v16, 0xd1, v239
	s_nop 0
	v_cndmask_b32_e32 v90, v227, v108, vcc
	v_cmp_le_i32_e32 vcc, v16, v238
	v_or_b32_e32 v16, 0xf1, v239
	s_nop 0
	v_cndmask_b32_e32 v107, v227, v91, vcc
	v_cmp_le_i32_e32 vcc, v16, v238
	v_or_b32_e32 v16, 0xd2, v239
	s_nop 0
	v_cndmask_b32_e32 v91, v227, v109, vcc
	v_cmp_le_i32_e32 vcc, v16, v238
	v_or_b32_e32 v16, 0xf2, v239
	s_nop 0
	v_cndmask_b32_e32 v108, v227, v92, vcc
	v_cmp_le_i32_e32 vcc, v16, v238
	v_or_b32_e32 v16, 0xd3, v239
	s_nop 0
	v_cndmask_b32_e32 v92, v227, v110, vcc
	v_cmp_le_i32_e32 vcc, v16, v238
	v_or_b32_e32 v16, 0xf3, v239
	s_nop 0
	v_cndmask_b32_e32 v109, v227, v93, vcc
	v_cmp_le_i32_e32 vcc, v16, v238
	v_or_b32_e32 v16, 0xd8, v239
	s_nop 0
	v_cndmask_b32_e32 v93, v227, v111, vcc
	v_cmp_le_i32_e32 vcc, v16, v238
	v_or_b32_e32 v16, 0xf8, v239
	s_nop 0
	v_cndmask_b32_e32 v110, v227, v94, vcc
	v_cmp_le_i32_e32 vcc, v16, v238
	v_or_b32_e32 v16, 0xd9, v239
	s_nop 0
	v_cndmask_b32_e32 v94, v227, v112, vcc
	v_cmp_le_i32_e32 vcc, v16, v238
	v_or_b32_e32 v16, 0xf9, v239
	s_nop 0
	v_cndmask_b32_e32 v111, v227, v95, vcc
	v_cmp_le_i32_e32 vcc, v16, v238
	v_or_b32_e32 v16, 0xda, v239
	s_nop 0
	v_cndmask_b32_e32 v95, v227, v113, vcc
	v_cmp_le_i32_e32 vcc, v16, v238
	v_or_b32_e32 v16, 0xfa, v239
	s_nop 0
	v_cndmask_b32_e32 v112, v227, v96, vcc
	v_cmp_le_i32_e32 vcc, v16, v238
	v_or_b32_e32 v16, 0xdb, v239
	s_nop 0
	v_cndmask_b32_e32 v96, v227, v114, vcc
	v_cmp_le_i32_e32 vcc, v16, v238
	v_sub_u32_e32 v16, v238, v239
	v_lshl_add_u32 v145, v16, 2, s40
	v_cndmask_b32_e32 v113, v227, v97, vcc
	v_or_b32_e32 v97, 0xfb, v239
	v_cmp_le_i32_e32 vcc, v97, v238
	ds_read2_b32 v[16:17], v145 offset0:63 offset1:64
	ds_read2_b32 v[84:85], v145 offset0:31 offset1:32
	v_cndmask_b32_e32 v97, v227, v115, vcc
	ds_read2_b32 v[114:115], v145 offset0:61 offset1:62
	ds_read2_b32 v[128:129], v145 offset0:29 offset1:30
	s_waitcnt lgkmcnt(3)
	v_add_f32_e32 v98, v82, v17
	s_waitcnt lgkmcnt(2)
	v_add_f32_e32 v82, v99, v85
	v_add_f32_e32 v99, v83, v16
	v_add_f32_e32 v83, v100, v84
	s_waitcnt lgkmcnt(1)
	v_add_f32_e32 v100, v101, v115
	s_waitcnt lgkmcnt(0)
	v_add_f32_e32 v84, v142, v129
	v_add_f32_e32 v101, v143, v114
	v_add_f32_e32 v85, v144, v128
	s_nop 0
	ds_read2_b32 v[16:17], v145 offset0:55 offset1:56
	ds_read2_b32 v[114:115], v145 offset0:23 offset1:24
	ds_read2_b32 v[128:129], v145 offset0:53 offset1:54
	ds_read2_b32 v[142:143], v145 offset0:21 offset1:22
	s_waitcnt lgkmcnt(3)
	v_add_f32_e32 v102, v102, v17
	s_waitcnt lgkmcnt(2)
	v_add_f32_e32 v86, v86, v115
	v_add_f32_e32 v103, v103, v16
	v_add_f32_e32 v87, v87, v114
	s_waitcnt lgkmcnt(1)
	v_add_f32_e32 v104, v104, v129
	s_waitcnt lgkmcnt(0)
	v_add_f32_e32 v88, v88, v143
	v_add_f32_e32 v105, v105, v128
	v_add_f32_e32 v89, v89, v142
	s_nop 0
	ds_read2_b32 v[16:17], v145 offset0:47 offset1:48
	ds_read2_b32 v[114:115], v145 offset0:15 offset1:16
	ds_read2_b32 v[128:129], v145 offset0:45 offset1:46
	ds_read2_b32 v[142:143], v145 offset0:13 offset1:14
	s_waitcnt lgkmcnt(3)
	v_add_f32_e32 v106, v106, v17
	s_waitcnt lgkmcnt(2)
	v_add_f32_e32 v90, v90, v115
	v_add_f32_e32 v107, v107, v16
	v_add_f32_e32 v91, v91, v114
	s_waitcnt lgkmcnt(1)
	v_add_f32_e32 v108, v108, v129
	s_waitcnt lgkmcnt(0)
	v_add_f32_e32 v92, v92, v143
	v_add_f32_e32 v109, v109, v128
	v_add_f32_e32 v93, v93, v142
	s_nop 0
	ds_read2_b32 v[16:17], v145 offset0:39 offset1:40
	ds_read2_b32 v[114:115], v145 offset0:7 offset1:8
	ds_read2_b32 v[128:129], v145 offset0:37 offset1:38
	ds_read2_b32 v[142:143], v145 offset0:5 offset1:6
	s_waitcnt lgkmcnt(3)
	v_add_f32_e32 v110, v110, v17
	s_waitcnt lgkmcnt(2)
	v_add_f32_e32 v94, v94, v115
	v_add_f32_e32 v111, v111, v16
	v_add_f32_e32 v95, v95, v114
	s_waitcnt lgkmcnt(1)
	v_add_f32_e32 v112, v112, v129
	s_waitcnt lgkmcnt(0)
	v_add_f32_e32 v96, v96, v143
	v_add_f32_e32 v113, v113, v128
	v_add_f32_e32 v97, v97, v142
	s_nop 0
	s_nop 0
	v_max_f32_e32 v16, v99, v98
	v_max3_f32 v17, v100, v101, v83
	v_max3_f32 v16, v16, v82, v84
	v_max3_f32 v16, v16, v85, v102
	v_max3_f32 v17, v17, v104, v105
	v_max3_f32 v16, v16, v103, v86
	v_max3_f32 v17, v17, v88, v89
	v_max3_f32 v16, v16, v87, v106
	v_max3_f32 v17, v17, v108, v109
	v_max3_f32 v16, v16, v107, v90
	v_max3_f32 v17, v17, v92, v93
	v_max3_f32 v16, v16, v91, v110
	v_max3_f32 v17, v17, v112, v113
	v_max3_f32 v16, v16, v111, v94
	v_max3_f32 v17, v17, v96, v97
	v_max3_f32 v16, v16, v95, v17
	v_mov_b32_e32 v17, v16
	s_nop 1
	v_permlane32_swap_b32_e32 v16, v17
	v_max_f32_e32 v16, v16, v17
	v_cmp_lt_f32_e32 vcc, s79, v16
	s_cmp_lg_u64 vcc, 0
	s_cselect_b64 s[0:1], -1, 0
	s_cbranch_vccnz .LBB0_346

.LBB0_952:
	v_add_u32_e32 v2, s43, v242
	ds_read_b64_tr_b16 v[194:195], v2 offset:24576
	ds_read_b64_tr_b16 v[196:197], v2 offset:25088
	s_waitcnt lgkmcnt(9)
	v_mfma_f32_32x32x16_bf16 v[82:97], v[170:173], v[154:157], v[100:115]
	ds_read_b64_tr_b16 v[170:171], v2 offset:28672
	ds_read_b64_tr_b16 v[172:173], v2 offset:29184
	s_waitcnt lgkmcnt(10)
	v_mfma_f32_32x32x16_bf16 v[100:115], v[162:165], v[154:157], v[100:115]
	ds_read_b64_tr_b16 v[124:125], v2 offset:25600
	ds_read_b64_tr_b16 v[126:127], v2 offset:26112
	s_waitcnt lgkmcnt(11)
	v_mfma_f32_32x32x16_bf16 v[82:97], v[174:177], v[150:153], v[82:97]
	ds_read_b64_tr_b16 v[120:121], v2 offset:29696
	ds_read_b64_tr_b16 v[122:123], v2 offset:30208
	s_waitcnt lgkmcnt(12)
	v_mfma_f32_32x32x16_bf16 v[100:115], v[166:169], v[150:153], v[100:115]
	ds_read_b64_tr_b16 v[116:117], v2 offset:26624
	ds_read_b64_tr_b16 v[118:119], v2 offset:27136
	s_waitcnt lgkmcnt(13)
	v_mfma_f32_32x32x16_bf16 v[82:97], v[182:185], v[146:149], v[82:97]
	ds_read_b64_tr_b16 v[12:13], v2 offset:30720
	ds_read_b64_tr_b16 v[14:15], v2 offset:31232
	s_waitcnt lgkmcnt(14)
	v_mfma_f32_32x32x16_bf16 v[100:115], v[178:181], v[146:149], v[100:115]
	ds_read_b64_tr_b16 v[8:9], v2 offset:27648
	ds_read_b64_tr_b16 v[10:11], v2 offset:28160
	s_waitcnt lgkmcnt(14)
	v_mfma_f32_32x32x16_bf16 v[82:97], v[190:193], v[142:145], v[82:97]
	ds_read_b64_tr_b16 v[4:5], v2 offset:31744
	ds_read_b64_tr_b16 v[6:7], v2 offset:32256
	v_mfma_f32_32x32x16_bf16 v[100:115], v[186:189], v[142:145], v[100:115]
	s_cmp_lt_u32 s21, 3
	s_cbranch_scc0 .Lpf_skip_l1
	v_readfirstlane_b32 s98, v0
	s_add_i32 s99, s21, 1
	s_lshr_b32 vcc_hi, s99, 1
	s_lshl_b32 vcc_hi, vcc_hi, 7
	s_bitcmp0_b32 s99, 0
	s_cselect_b32 s99, s50, s47
	s_ashr_i32 s98, s98, 6
	s_mul_i32 vcc_lo, s4, 0x4800000
	s_lshl_b32 s99, s99, 8
	s_lshl_b32 s100, s4, 14
	s_add_i32 s99, s99, s100
	s_lshl_b32 s100, s98, 5
	s_add_i32 s99, s99, s100
	s_mul_i32 s99, s99, 0x1200
	s_add_u32 s100, s51, vcc_hi
	s_addc_u32 s101, s52, 0
	s_add_u32 s100, s100, s99
	s_addc_u32 s101, s101, 0
	v_and_b32_e32 v244, 31, v0
	v_mul_u32_u24_e32 v244, 0x1200, v244
	v_bfe_u32 v245, v0, 5, 1
	v_lshl_or_b32 v244, v245, 4, v244
	global_load_dword v198, v244, s[100:101]
	s_add_u32 s100, s53, vcc_hi
	s_addc_u32 s101, s55, 0
	s_add_u32 s100, s100, vcc_lo
	s_addc_u32 s101, s101, 0
	s_lshl_b32 s99, s98, 4
	s_add_u32 s100, s100, s99
	s_addc_u32 s101, s101, 0
	v_and_b32_e32 v245, 63, v0
	v_mul_u32_u24_e32 v245, 0x1200, v245
	global_load_dword v199, v245, s[100:101]
	s_add_u32 s100, s100, 0x48000
	s_addc_u32 s101, s101, 0
	global_load_dword v200, v245, s[100:101]
	s_add_u32 s100, s56, vcc_lo
	s_addc_u32 s101, s57, 0
	s_lshr_b32 s99, s98, 2
	s_lshl_b32 s99, s99, 6
	s_add_u32 s100, s100, s99
	s_addc_u32 s101, s101, 0
	s_and_b32 s99, s98, 3
	s_lshl_b32 s99, s99, 4
	v_bfe_u32 v246, v0, 2, 4
	v_add_u32_e32 v246, s99, v246
	v_mul_u32_u24_e32 v246, 0x1200, v246
	v_and_b32_e32 v247, 3, v0
	v_lshl_add_u32 v246, v247, 4, v246
	global_load_dword v201, v246, s[100:101]
	global_load_dword v202, v246, s[100:101] offset:128
.Lpf_skip_l1:
	v_or_b32_e32 v17, 0xe0, v239
	v_or_b32_e32 v16, 0xc0, v239
	v_cmp_le_i32_e32 vcc, v17, v238
	s_nop 8
	v_cndmask_b32_e32 v99, v227, v100, vcc
	v_cmp_lt_i32_e32 vcc, v16, v238
	s_nop 1
	v_cndmask_b32_e32 v83, v227, v83, vcc
	v_cmp_le_i32_e32 vcc, v16, v238
	v_or_b32_e32 v16, 0xe1, v239
	s_nop 0
	v_cndmask_b32_e32 v82, v227, v82, vcc
	v_cmp_le_i32_e32 vcc, v16, v238
	v_or_b32_e32 v16, 0xc2, v239
	s_nop 0
	v_cndmask_b32_e32 v100, v227, v101, vcc
	v_cmp_le_i32_e32 vcc, v16, v238
	v_or_b32_e32 v16, 0xe2, v239
	s_nop 0
	v_cndmask_b32_e32 v101, v227, v84, vcc
	v_cmp_le_i32_e32 vcc, v16, v238
	v_or_b32_e32 v16, 0xc3, v239
	s_nop 0
	v_cndmask_b32_e32 v142, v227, v102, vcc
	v_cmp_le_i32_e32 vcc, v16, v238
	v_or_b32_e32 v16, 0xe3, v239
	s_nop 0
	v_cndmask_b32_e32 v143, v227, v85, vcc
	v_cmp_le_i32_e32 vcc, v16, v238
	v_or_b32_e32 v16, 0xc8, v239
	s_nop 0
	v_cndmask_b32_e32 v144, v227, v103, vcc
	v_cmp_le_i32_e32 vcc, v16, v238
	v_or_b32_e32 v16, 0xe8, v239
	s_nop 0
	v_cndmask_b32_e32 v102, v227, v86, vcc
	v_cmp_le_i32_e32 vcc, v16, v238
	v_or_b32_e32 v16, 0xc9, v239
	s_nop 0
	v_cndmask_b32_e32 v86, v227, v104, vcc
	v_cmp_le_i32_e32 vcc, v16, v238
	v_or_b32_e32 v16, 0xe9, v239
	s_nop 0
	v_cndmask_b32_e32 v103, v227, v87, vcc
	v_cmp_le_i32_e32 vcc, v16, v238
	v_or_b32_e32 v16, 0xca, v239
	s_nop 0
	v_cndmask_b32_e32 v87, v227, v105, vcc
	v_cmp_le_i32_e32 vcc, v16, v238
	v_or_b32_e32 v16, 0xea, v239
	s_nop 0
	v_cndmask_b32_e32 v104, v227, v88, vcc
	v_cmp_le_i32_e32 vcc, v16, v238
	v_or_b32_e32 v16, 0xcb, v239
	s_nop 0
	v_cndmask_b32_e32 v88, v227, v106, vcc
	v_cmp_le_i32_e32 vcc, v16, v238
	v_or_b32_e32 v16, 0xeb, v239
	s_nop 0
	v_cndmask_b32_e32 v105, v227, v89, vcc
	v_cmp_le_i32_e32 vcc, v16, v238
	v_or_b32_e32 v16, 0xd0, v239
	s_nop 0
	v_cndmask_b32_e32 v89, v227, v107, vcc
	v_cmp_le_i32_e32 vcc, v16, v238
	v_or_b32_e32 v16, 0xf0, v239
	s_nop 0
	v_cndmask_b32_e32 v106, v227, v90, vcc
	v_cmp_le_i32_e32 vcc, v16, v238
	v_or_b32_e32 v16, 0xd1, v239
	s_nop 0
	v_cndmask_b32_e32 v90, v227, v108, vcc
	v_cmp_le_i32_e32 vcc, v16, v238
	v_or_b32_e32 v16, 0xf1, v239
	s_nop 0
	v_cndmask_b32_e32 v107, v227, v91, vcc
	v_cmp_le_i32_e32 vcc, v16, v238
	v_or_b32_e32 v16, 0xd2, v239
	s_nop 0
	v_cndmask_b32_e32 v91, v227, v109, vcc
	v_cmp_le_i32_e32 vcc, v16, v238
	v_or_b32_e32 v16, 0xf2, v239
	s_nop 0
	v_cndmask_b32_e32 v108, v227, v92, vcc
	v_cmp_le_i32_e32 vcc, v16, v238
	v_or_b32_e32 v16, 0xd3, v239
	s_nop 0
	v_cndmask_b32_e32 v92, v227, v110, vcc
	v_cmp_le_i32_e32 vcc, v16, v238
	v_or_b32_e32 v16, 0xf3, v239
	s_nop 0
	v_cndmask_b32_e32 v109, v227, v93, vcc
	v_cmp_le_i32_e32 vcc, v16, v238
	v_or_b32_e32 v16, 0xd8, v239
	s_nop 0
	v_cndmask_b32_e32 v93, v227, v111, vcc
	v_cmp_le_i32_e32 vcc, v16, v238
	v_or_b32_e32 v16, 0xf8, v239
	s_nop 0
	v_cndmask_b32_e32 v110, v227, v94, vcc
	v_cmp_le_i32_e32 vcc, v16, v238
	v_or_b32_e32 v16, 0xd9, v239
	s_nop 0
	v_cndmask_b32_e32 v94, v227, v112, vcc
	v_cmp_le_i32_e32 vcc, v16, v238
	v_or_b32_e32 v16, 0xf9, v239
	s_nop 0
	v_cndmask_b32_e32 v111, v227, v95, vcc
	v_cmp_le_i32_e32 vcc, v16, v238
	v_or_b32_e32 v16, 0xda, v239
	s_nop 0
	v_cndmask_b32_e32 v95, v227, v113, vcc
	v_cmp_le_i32_e32 vcc, v16, v238
	v_or_b32_e32 v16, 0xfa, v239
	s_nop 0
	v_cndmask_b32_e32 v112, v227, v96, vcc
	v_cmp_le_i32_e32 vcc, v16, v238
	v_or_b32_e32 v16, 0xdb, v239
	s_nop 0
	v_cndmask_b32_e32 v96, v227, v114, vcc
	v_cmp_le_i32_e32 vcc, v16, v238
	v_sub_u32_e32 v16, v238, v239
	v_lshl_add_u32 v145, v16, 2, s40
	v_cndmask_b32_e32 v113, v227, v97, vcc
	v_or_b32_e32 v97, 0xfb, v239
	v_cmp_le_i32_e32 vcc, v97, v238
	ds_read2_b32 v[16:17], v145 offset0:63 offset1:64
	ds_read2_b32 v[84:85], v145 offset0:31 offset1:32
	v_cndmask_b32_e32 v97, v227, v115, vcc
	ds_read2_b32 v[114:115], v145 offset0:61 offset1:62
	ds_read2_b32 v[128:129], v145 offset0:29 offset1:30
	s_waitcnt lgkmcnt(3)
	v_add_f32_e32 v98, v82, v17
	s_waitcnt lgkmcnt(2)
	v_add_f32_e32 v82, v99, v85
	v_add_f32_e32 v99, v83, v16
	v_add_f32_e32 v83, v100, v84
	s_waitcnt lgkmcnt(1)
	v_add_f32_e32 v100, v101, v115
	s_waitcnt lgkmcnt(0)
	v_add_f32_e32 v84, v142, v129
	v_add_f32_e32 v101, v143, v114
	v_add_f32_e32 v85, v144, v128
	s_nop 0
	ds_read2_b32 v[16:17], v145 offset0:55 offset1:56
	ds_read2_b32 v[114:115], v145 offset0:23 offset1:24
	ds_read2_b32 v[128:129], v145 offset0:53 offset1:54
	ds_read2_b32 v[142:143], v145 offset0:21 offset1:22
	s_waitcnt lgkmcnt(3)
	v_add_f32_e32 v102, v102, v17
	s_waitcnt lgkmcnt(2)
	v_add_f32_e32 v86, v86, v115
	v_add_f32_e32 v103, v103, v16
	v_add_f32_e32 v87, v87, v114
	s_waitcnt lgkmcnt(1)
	v_add_f32_e32 v104, v104, v129
	s_waitcnt lgkmcnt(0)
	v_add_f32_e32 v88, v88, v143
	v_add_f32_e32 v105, v105, v128
	v_add_f32_e32 v89, v89, v142
	s_nop 0
	ds_read2_b32 v[16:17], v145 offset0:47 offset1:48
	ds_read2_b32 v[114:115], v145 offset0:15 offset1:16
	ds_read2_b32 v[128:129], v145 offset0:45 offset1:46
	ds_read2_b32 v[142:143], v145 offset0:13 offset1:14
	s_waitcnt lgkmcnt(3)
	v_add_f32_e32 v106, v106, v17
	s_waitcnt lgkmcnt(2)
	v_add_f32_e32 v90, v90, v115
	v_add_f32_e32 v107, v107, v16
	v_add_f32_e32 v91, v91, v114
	s_waitcnt lgkmcnt(1)
	v_add_f32_e32 v108, v108, v129
	s_waitcnt lgkmcnt(0)
	v_add_f32_e32 v92, v92, v143
	v_add_f32_e32 v109, v109, v128
	v_add_f32_e32 v93, v93, v142
	s_nop 0
	ds_read2_b32 v[16:17], v145 offset0:39 offset1:40
	ds_read2_b32 v[114:115], v145 offset0:7 offset1:8
	ds_read2_b32 v[128:129], v145 offset0:37 offset1:38
	ds_read2_b32 v[142:143], v145 offset0:5 offset1:6
	s_waitcnt lgkmcnt(3)
	v_add_f32_e32 v110, v110, v17
	s_waitcnt lgkmcnt(2)
	v_add_f32_e32 v94, v94, v115
	v_add_f32_e32 v111, v111, v16
	v_add_f32_e32 v95, v95, v114
	s_waitcnt lgkmcnt(1)
	v_add_f32_e32 v112, v112, v129
	s_waitcnt lgkmcnt(0)
	v_add_f32_e32 v96, v96, v143
	v_add_f32_e32 v113, v113, v128
	v_add_f32_e32 v97, v97, v142
	s_nop 0
	s_nop 0
	v_max_f32_e32 v16, v99, v98
	v_max3_f32 v17, v100, v101, v83
	v_max3_f32 v16, v16, v82, v84
	v_max3_f32 v16, v16, v85, v102
	v_max3_f32 v17, v17, v104, v105
	v_max3_f32 v16, v16, v103, v86
	v_max3_f32 v17, v17, v88, v89
	v_max3_f32 v16, v16, v87, v106
	v_max3_f32 v17, v17, v108, v109
	v_max3_f32 v16, v16, v107, v90
	v_max3_f32 v17, v17, v92, v93
	v_max3_f32 v16, v16, v91, v110
	v_max3_f32 v17, v17, v112, v113
	v_max3_f32 v16, v16, v111, v94
	v_max3_f32 v17, v17, v96, v97
	v_max3_f32 v16, v16, v95, v17
	v_mov_b32_e32 v17, v16
	s_nop 1
	v_permlane32_swap_b32_e32 v16, v17
	v_max_f32_e32 v16, v16, v17
	v_cmp_lt_f32_e32 vcc, s60, v16
	s_cmp_lg_u64 vcc, 0
	s_cselect_b64 s[0:1], -1, 0
	s_cbranch_vccnz .LBB0_959

.LBB0_959:
	v_max_f32_e32 v16, v16, v16
	v_max_f32_e32 v17, 0, v16
	v_exp_f32_e64 v16, -v17
	v_cmp_gt_u32_e32 vcc, 32, v230
	s_and_saveexec_b64 s[2:3], vcc
	ds_write_b32 v235, v16
	s_or_b64 exec, exec, s[2:3]
	v_sub_f32_e32 v113, v113, v17
	v_sub_f32_e32 v112, v112, v17
	v_sub_f32_e32 v111, v111, v17
	v_sub_f32_e32 v110, v110, v17
	v_sub_f32_e32 v109, v109, v17
	v_sub_f32_e32 v108, v108, v17
	v_sub_f32_e32 v107, v107, v17
	v_sub_f32_e32 v106, v106, v17
	v_sub_f32_e32 v105, v105, v17
	v_sub_f32_e32 v104, v104, v17
	v_sub_f32_e32 v103, v103, v17
	v_sub_f32_e32 v102, v102, v17
	v_sub_f32_e32 v101, v101, v17
	v_sub_f32_e32 v100, v100, v17
	v_sub_f32_e32 v99, v99, v17
	v_sub_f32_e32 v98, v98, v17
	v_sub_f32_e32 v97, v97, v17
	v_sub_f32_e32 v96, v96, v17
	v_sub_f32_e32 v95, v95, v17
	v_sub_f32_e32 v94, v94, v17
	v_sub_f32_e32 v93, v93, v17
	v_sub_f32_e32 v92, v92, v17
	v_sub_f32_e32 v91, v91, v17
	v_sub_f32_e32 v90, v90, v17
	v_sub_f32_e32 v89, v89, v17
	v_sub_f32_e32 v88, v88, v17
	v_sub_f32_e32 v87, v87, v17
	v_sub_f32_e32 v86, v86, v17
	v_sub_f32_e32 v85, v85, v17
	v_sub_f32_e32 v84, v84, v17
	v_sub_f32_e32 v83, v83, v17
	v_sub_f32_e32 v82, v82, v17
	v_mul_f32_e32 v243, v243, v16
	s_branch .LBB0_953
	s_nop 0
	s_nop 0
	s_nop 0
	s_nop 0
	s_nop 0
	s_nop 0
	s_nop 0
	s_nop 0
	s_nop 0
	s_nop 0
	s_nop 0
	s_nop 0
	s_nop 0
